# global wave index = ((wave>>2)*G + vcu)*4 + (wave&3): groups of four waves keep adjacent tasks, groups interleaved across CUs
# speedup vs baseline: 1.0046x; 1.0013x over previous
.LBB0_13:
	v_writelane_b32 v251, s12, 16
	v_writelane_b32 v251, s10, 18
	s_nop 1
	v_writelane_b32 v251, s11, 19
	s_or_b64 exec, exec, s[2:3]
	s_load_dwordx16 s[36:51], s[0:1], 0x0
	s_load_dword s3, s[0:1], 0xe0
	v_readlane_b32 s5, v251, 4
	s_lshr_b32 s8, s6, 6
	s_nop 0
	s_nop 0
	v_writelane_b32 v251, s8, 20
	s_nop 0
	s_waitcnt lgkmcnt(0)
	s_lshr_b32 s2, s8, 2
	s_mul_i32 s2, s2, s3
	s_add_i32 s2, s2, s5
	s_lshl_b32 s2, s2, 2
	s_and_b32 s4, s8, 3
	s_add_i32 s4, s2, s4
	s_mov_b32 s2, s4
	s_lshl_b32 s17, s3, 3
	v_writelane_b32 v251, s2, 21
	s_mov_b32 s16, s4
	v_mov_b32_e32 v50, v246
	v_writelane_b32 v251, s3, 22
	v_writelane_b32 v251, s17, 23
	s_movk_i32 s2, 0x1400
	s_mov_b32 s28, s5
	v_writelane_b32 v251, s3, 24
	v_cmp_gt_i32_e32 vcc, s2, v50
	s_and_saveexec_b64 s[2:3], vcc
	s_cbranch_execz .LBB0_16
	v_mov_b32_e32 v2, s38
	v_mov_b32_e32 v3, s39
	v_ashrrev_i32_e32 v51, 31, v50
	v_lshl_add_u32 v1, v50, 2, 0
	v_lshl_add_u64 v[2:3], v[50:51], 2, v[2:3]
	s_mov_b64 s[4:5], 0
	s_movk_i32 s9, 0x1000
	v_mov_b32_e32 v5, 0
	s_mov_b64 s[6:7], 0x800
	s_movk_i32 s10, 0x11ff
	v_mov_b32_e32 v6, v50
